# conv/Fourier-A/attention phase: workgroups on odd XCDs run their attention units first and the streaming conv + Fourier stage A afterwards, so the memory-bound sub-phases of one half overlap the compu
# speedup vs baseline: 1.0014x; 1.0014x over previous
; #define PB_BEGIN(id) unsigned long long _pt0_##id = (((PROBE_MASK) >> (id)) & 1) ? __builtin_amdgcn_s_memrealtime() : 0ull
; #define PB_END(id) do { if (((PROBE_MASK) >> (id)) & 1) { __syncthreads(); const unsigned long long _t1 = __builtin_amdgcn_s_memrealtime(), _w = (_t1 - _pt0_##id) * (PROBE_MUL); \
;         while (__builtin_amdgcn_s_memrealtime() - _t1 < _w) __builtin_amdgcn_s_sleep(8); } } while (0)
; #define PB_BEGIN(id) do {} while (0)
; #define PB_END(id) do {} while (0)
; __global__ void __launch_bounds__(NTHR, 2) fwd_kernel(Params prm) {
;     ...
;             PB_BEGIN(3); launder(F); if (SUB3 & 1) phase_conv(F, P, l, nrows); launder(F); PB_END(3); PB_BEGIN(4);
;             if (SUB3 & 2) phase_fft_a(F);
;             launder(F); if ((SUB3 & 4) && l == 0) phase_ctx_dft(F); launder(F); PB_END(4); PB_BEGIN(5);
;             if (SUB3 & 8) phase_attn(F, P, l);
.LBB0_320:
	s_andn2_b64 vcc, exec, s[8:9]
	s_cbranch_vccnz .LBB0_506
	v_readlane_b32 s100, v254, 62
	s_nop 0
	s_bitcmp1_b32 s100, 0
	s_cbranch_scc0 .Lpb2_conv
	s_movk_i32 s22, 0x400
	s_andn2_b64 vcc, exec, s[64:65]
	s_cbranch_vccnz .Lpb2_attn_entry
	s_movk_i32 s22, 0x420
	s_branch .Lpb2_attn_entry
.Lpb2_conv:
	s_waitcnt vmcnt(0)
	v_mov_b32_e32 v2, v0
	v_readlane_b32 s0, v252, 6
	v_readlane_b32 s1, v252, 7
	v_ashrrev_i32_e32 v3, 31, v2
	s_nop 0
	v_lshl_add_u64 v[50:51], s[0:1], 0, v[2:3]
	v_readlane_b32 s0, v255, 13
	s_lshl_b32 s76, s0, 4
	v_cmp_gt_u64_e32 vcc, s[76:77], v[50:51]
	s_and_saveexec_b64 s[44:45], vcc
	v_readlane_b32 s8, v252, 52
	v_readlane_b32 s9, v252, 53
	s_movk_i32 s2, 0x1000
	v_readlane_b32 s7, v255, 1
	s_movk_i32 s18, 0x3000
	s_movk_i32 s19, 0x5000
	s_mov_b64 s[22:23], 0x100000
	s_cbranch_execz .LBB0_324
	v_readlane_b32 s0, v255, 9
	v_readlane_b32 s1, v255, 10
	s_mulk_i32 s0, 0x600
	s_mov_b32 s1, s77
	v_readlane_b32 s28, v254, 52
	s_lshl_b64 s[0:1], s[0:1], 2
	v_readlane_b32 s30, v254, 54
	v_readlane_b32 s31, v254, 55
	s_add_u32 s46, s30, s0
	s_addc_u32 s47, s31, s1
	s_add_u32 s48, s56, 0x1c316100
	v_readlane_b32 s0, v252, 6
	s_addc_u32 s49, s57, 0
	s_mov_b64 s[50:51], 0
	v_add_lshl_u32 v1, s0, v2, 3
	v_readlane_b32 s29, v254, 53
	v_readlane_b32 s1, v252, 7

; #define SEAM(k) do { if (IN((k) + 1)) { xcd_barrier(bar); xcd_barrier(bar); } } while (0)
; #define SEAM(k) do { if (IN((k) + 1)) xcd_barrier(bar); } while (0)
; #define PB_BEGIN(id) unsigned long long _pt0_##id = (((PROBE_MASK) >> (id)) & 1) ? __builtin_amdgcn_s_memrealtime() : 0ull
; #define PB_END(id) do { if (((PROBE_MASK) >> (id)) & 1) { __syncthreads(); const unsigned long long _t1 = __builtin_amdgcn_s_memrealtime(), _w = (_t1 - _pt0_##id) * (PROBE_MUL); \
;         while (__builtin_amdgcn_s_memrealtime() - _t1 < _w) __builtin_amdgcn_s_sleep(8); } } while (0)
; #define PB_BEGIN(id) do {} while (0)
; #define PB_END(id) do {} while (0)
; __global__ void __launch_bounds__(NTHR, 2) fwd_kernel(Params prm) {
;     ...
;             PB_BEGIN(3); launder(F); if (SUB3 & 1) phase_conv(F, P, l, nrows); launder(F); PB_END(3); PB_BEGIN(4);
;             if (SUB3 & 2) phase_fft_a(F);
;             launder(F); if ((SUB3 & 4) && l == 0) phase_ctx_dft(F); launder(F); PB_END(4); PB_BEGIN(5);
;             if (SUB3 & 8) phase_attn(F, P, l);
;             PB_END(5);
;             SEAM(PB + 2);
.LBB0_338:
	v_readlane_b32 s100, v254, 62
	s_nop 0
	s_bitcmp1_b32 s100, 0
	s_cbranch_scc0 .Lpb2_attn_entry
	v_readlane_b32 s7, v245, 0
	v_readlane_b32 s24, v245, 1
	v_readlane_b32 s25, v245, 2
	v_readlane_b32 s28, v245, 3
	v_readlane_b32 s29, v245, 4
	v_readlane_b32 s30, v245, 5
	v_readlane_b32 s31, v245, 6
	v_readlane_b32 s40, v245, 7
	v_readlane_b32 s41, v245, 8
	v_readlane_b32 s42, v245, 9
	v_readlane_b32 s43, v245, 10
	v_readlane_b32 s46, v245, 11
	v_readlane_b32 s47, v245, 12
	v_readlane_b32 s48, v245, 13
	v_readlane_b32 s49, v245, 14
	v_readlane_b32 s50, v245, 15
	v_readlane_b32 s51, v245, 16
	v_readlane_b32 s76, v245, 17
	v_mov_b32_e32 v198, v0
	s_nop 4
	s_branch .Lpb2_seam

; #define SEAM(k) do { if (IN((k) + 1)) { xcd_barrier(bar); xcd_barrier(bar); } } while (0)
; #define SEAM(k) do { if (IN((k) + 1)) xcd_barrier(bar); } while (0)
; #define PB_BEGIN(id) unsigned long long _pt0_##id = (((PROBE_MASK) >> (id)) & 1) ? __builtin_amdgcn_s_memrealtime() : 0ull
; #define PB_END(id) do { if (((PROBE_MASK) >> (id)) & 1) { __syncthreads(); const unsigned long long _t1 = __builtin_amdgcn_s_memrealtime(), _w = (_t1 - _pt0_##id) * (PROBE_MUL); \
;         while (__builtin_amdgcn_s_memrealtime() - _t1 < _w) __builtin_amdgcn_s_sleep(8); } } while (0)
; #define PB_BEGIN(id) do {} while (0)
; #define PB_END(id) do {} while (0)
; __global__ void __launch_bounds__(NTHR, 2) fwd_kernel(Params prm) {
;     ...
;             launder(F); if ((SUB3 & 4) && l == 0) phase_ctx_dft(F); launder(F); PB_END(4); PB_BEGIN(5);
;             if (SUB3 & 8) phase_attn(F, P, l);
;             PB_END(5);
;             SEAM(PB + 2);
.LBB0_456:
	v_readlane_b32 s100, v254, 62
	s_nop 0
	s_bitcmp1_b32 s100, 0
	s_cbranch_scc0 .Lpb2_seam
	v_writelane_b32 v245, s7, 0
	v_writelane_b32 v245, s24, 1
	v_writelane_b32 v245, s25, 2
	v_writelane_b32 v245, s28, 3
	v_writelane_b32 v245, s29, 4
	v_writelane_b32 v245, s30, 5
	v_writelane_b32 v245, s31, 6
	v_writelane_b32 v245, s40, 7
	v_writelane_b32 v245, s41, 8
	v_writelane_b32 v245, s42, 9
	v_writelane_b32 v245, s43, 10
	v_writelane_b32 v245, s46, 11
	v_writelane_b32 v245, s47, 12
	v_writelane_b32 v245, s48, 13
	v_writelane_b32 v245, s49, 14
	v_writelane_b32 v245, s50, 15
	v_writelane_b32 v245, s51, 16
	v_writelane_b32 v245, s76, 17
	s_waitcnt lgkmcnt(0)
	s_barrier
	s_branch .Lpb2_conv
